# GEMM unit boundary: leading half no longer idles at the align barrier; its epilogue + next L segment overlap the trailing half's last MFMA segment + epilogue (one barrier less per half per unit)
# speedup vs baseline: 1.0010x; 1.0010x over previous
.LBB0_265:
	s_cmp_eq_u32 s58, 60
	s_cselect_b32 s100, 1, 0
	s_cmp_eq_u64 s[30:31], 0
	s_cselect_b32 s101, 1, 0
	s_and_b32 s100, s100, s101
	s_add_u32 s24, s6, 0xfff00080
	s_addc_u32 s25, s7, -1
	s_add_i32 s28, 0, 0x10000
	s_cmp_eq_u32 s58, 60
	s_cselect_b32 s27, s73, s25
	s_cselect_b32 s26, vcc_lo, s24
	s_cselect_b32 s25, s75, s13
	s_cselect_b32 s24, vcc_hi, s21
	s_add_i32 s71, 0, 0x14000
	v_add_u32_e32 v144, s28, v163
	v_add_u32_e32 v182, s71, v163
	s_waitcnt lgkmcnt(0)
	ds_read_b128 v[132:135], v144
	ds_read_b128 v[136:139], v144 offset:1024
	ds_read_b128 v[140:143], v144 offset:2048
	ds_read_b128 v[144:147], v144 offset:3072
	ds_read_b128 v[148:151], v182
	ds_read_b128 v[152:155], v182 offset:1024
	ds_read_b128 v[178:181], v182 offset:2048
	ds_read_b128 v[186:189], v182 offset:3072
	v_lshl_add_u64 v[182:183], s[6:7], 0, v[174:175]
	s_add_i32 m0, s46, 0xc000
	ds_read_b128 v[190:193], v184
	ds_read_b128 v[194:197], v184 offset:1024
	ds_read_b128 v[198:201], v184 offset:2048
	ds_read_b128 v[202:205], v184 offset:3072
	ds_read_b128 v[222:225], v184 offset:4096
	ds_read_b128 v[226:229], v184 offset:5120
	ds_read_b128 v[230:233], v184 offset:6144
	ds_read_b128 v[234:237], v184 offset:7168
	global_load_lds_dwordx4 v[182:183], off
	v_lshl_add_u64 v[182:183], s[6:7], 0, v[176:177]
	s_add_i32 m0, s46, 0xe000
	s_nop 0
	global_load_lds_dwordx4 v[182:183], off
	s_waitcnt vmcnt(8)
	s_waitcnt lgkmcnt(0)
	s_setprio 1
	s_barrier
	v_mfma_f32_16x16x32_bf16 v[120:123], v[132:135], v[190:193], v[120:123]
	v_mfma_f32_16x16x32_bf16 v[116:119], v[140:143], v[190:193], v[116:119]
	v_mfma_f32_16x16x32_bf16 v[104:107], v[132:135], v[198:201], v[104:107]
	v_mfma_f32_16x16x32_bf16 v[100:103], v[140:143], v[198:201], v[100:103]
	v_mfma_f32_16x16x32_bf16 v[88:91], v[132:135], v[222:225], v[88:91]
	v_mfma_f32_16x16x32_bf16 v[84:87], v[140:143], v[222:225], v[84:87]
	v_mfma_f32_16x16x32_bf16 v[72:75], v[132:135], v[230:233], v[72:75]
	v_mfma_f32_16x16x32_bf16 v[68:71], v[140:143], v[230:233], v[68:71]
	v_mfma_f32_16x16x32_bf16 v[120:123], v[136:139], v[194:197], v[120:123]
	v_mfma_f32_16x16x32_bf16 v[116:119], v[144:147], v[194:197], v[116:119]
	v_mfma_f32_16x16x32_bf16 v[104:107], v[136:139], v[202:205], v[104:107]
	v_mfma_f32_16x16x32_bf16 v[100:103], v[144:147], v[202:205], v[100:103]
	v_mfma_f32_16x16x32_bf16 v[88:91], v[136:139], v[226:229], v[88:91]
	v_mfma_f32_16x16x32_bf16 v[84:87], v[144:147], v[226:229], v[84:87]
	v_mfma_f32_16x16x32_bf16 v[72:75], v[136:139], v[234:237], v[72:75]
	v_mfma_f32_16x16x32_bf16 v[68:71], v[144:147], v[234:237], v[68:71]
	v_mfma_f32_16x16x32_bf16 v[128:131], v[148:151], v[190:193], v[128:131]
	v_mfma_f32_16x16x32_bf16 v[124:127], v[178:181], v[190:193], v[124:127]
	v_mfma_f32_16x16x32_bf16 v[112:115], v[148:151], v[198:201], v[112:115]
	v_mfma_f32_16x16x32_bf16 v[108:111], v[178:181], v[198:201], v[108:111]
	v_mfma_f32_16x16x32_bf16 v[96:99], v[148:151], v[222:225], v[96:99]
	v_mfma_f32_16x16x32_bf16 v[92:95], v[178:181], v[222:225], v[92:95]
	v_mfma_f32_16x16x32_bf16 v[80:83], v[148:151], v[230:233], v[80:83]
	v_mfma_f32_16x16x32_bf16 v[76:79], v[178:181], v[230:233], v[76:79]
	v_mfma_f32_16x16x32_bf16 v[128:131], v[152:155], v[194:197], v[128:131]
	v_mfma_f32_16x16x32_bf16 v[124:127], v[186:189], v[194:197], v[124:127]
	v_mfma_f32_16x16x32_bf16 v[112:115], v[152:155], v[202:205], v[112:115]
	v_mfma_f32_16x16x32_bf16 v[108:111], v[186:189], v[202:205], v[108:111]
	v_mfma_f32_16x16x32_bf16 v[96:99], v[152:155], v[226:229], v[96:99]
	v_mfma_f32_16x16x32_bf16 v[92:95], v[186:189], v[226:229], v[92:95]
	v_mfma_f32_16x16x32_bf16 v[80:83], v[152:155], v[234:237], v[80:83]
	v_mfma_f32_16x16x32_bf16 v[76:79], v[186:189], v[234:237], v[76:79]
	s_barrier
	s_setprio 0
	s_add_i32 s28, s28, s1
	v_lshl_add_u64 v[182:183], s[24:25], 0, v[2:3]
	s_mov_b32 m0, s28
	ds_read_b128 v[190:193], v184 offset:16384
	ds_read_b128 v[194:197], v184 offset:17408
	ds_read_b128 v[198:201], v184 offset:18432
	ds_read_b128 v[202:205], v184 offset:19456
	ds_read_b128 v[222:225], v184 offset:20480
	ds_read_b128 v[226:229], v184 offset:21504
	ds_read_b128 v[230:233], v184 offset:22528
	ds_read_b128 v[234:237], v184 offset:23552
	global_load_lds_dwordx4 v[182:183], off
	s_add_i32 m0, s28, 0x2000
	s_add_u32 s28, s24, 0x100000
	v_lshl_add_u64 v[238:239], s[24:25], 0, v[168:169]
	s_addc_u32 s29, s25, 0
	s_add_i32 s71, s71, s1
	global_load_lds_dwordx4 v[238:239], off
	v_lshl_add_u64 v[240:241], s[28:29], 0, v[2:3]
	s_mov_b32 m0, s71
	v_lshl_add_u64 v[242:243], s[26:27], 0, v[170:171]
	global_load_lds_dwordx4 v[240:241], off
	v_lshl_add_u64 v[240:241], s[28:29], 0, v[168:169]
	s_add_i32 m0, s71, 0x2000
	s_nop 0
	global_load_lds_dwordx4 v[240:241], off
	v_lshl_add_u64 v[240:241], s[26:27], 0, v[172:173]
	s_mov_b32 m0, s46
	s_nop 0
	global_load_lds_dwordx4 v[240:241], off
	s_mov_b32 m0, s50
	s_nop 0
	global_load_lds_dwordx4 v[242:243], off
	s_waitcnt vmcnt(8)
	s_waitcnt lgkmcnt(0)
	s_setprio 1
	s_barrier
	v_mfma_f32_16x16x32_bf16 v[56:59], v[132:135], v[190:193], v[56:59]
	v_mfma_f32_16x16x32_bf16 v[52:55], v[140:143], v[190:193], v[52:55]
	v_mfma_f32_16x16x32_bf16 v[40:43], v[132:135], v[198:201], v[40:43]
	v_mfma_f32_16x16x32_bf16 v[36:39], v[140:143], v[198:201], v[36:39]
	v_mfma_f32_16x16x32_bf16 v[24:27], v[132:135], v[222:225], v[24:27]
	v_mfma_f32_16x16x32_bf16 v[20:23], v[140:143], v[222:225], v[20:23]
	v_mfma_f32_16x16x32_bf16 v[8:11], v[132:135], v[230:233], v[8:11]
	v_mfma_f32_16x16x32_bf16 v[4:7], v[140:143], v[230:233], v[4:7]
	v_mfma_f32_16x16x32_bf16 v[56:59], v[136:139], v[194:197], v[56:59]
	v_mfma_f32_16x16x32_bf16 v[52:55], v[144:147], v[194:197], v[52:55]
	v_mfma_f32_16x16x32_bf16 v[40:43], v[136:139], v[202:205], v[40:43]
	v_mfma_f32_16x16x32_bf16 v[36:39], v[144:147], v[202:205], v[36:39]
	v_mfma_f32_16x16x32_bf16 v[24:27], v[136:139], v[226:229], v[24:27]
	v_mfma_f32_16x16x32_bf16 v[20:23], v[144:147], v[226:229], v[20:23]
	v_mfma_f32_16x16x32_bf16 v[8:11], v[136:139], v[234:237], v[8:11]
	v_mfma_f32_16x16x32_bf16 v[4:7], v[144:147], v[234:237], v[4:7]
	v_mfma_f32_16x16x32_bf16 v[64:67], v[148:151], v[190:193], v[64:67]
	v_mfma_f32_16x16x32_bf16 v[60:63], v[178:181], v[190:193], v[60:63]
	v_mfma_f32_16x16x32_bf16 v[48:51], v[148:151], v[198:201], v[48:51]
	v_mfma_f32_16x16x32_bf16 v[44:47], v[178:181], v[198:201], v[44:47]
	v_mfma_f32_16x16x32_bf16 v[32:35], v[148:151], v[222:225], v[32:35]
	v_mfma_f32_16x16x32_bf16 v[28:31], v[178:181], v[222:225], v[28:31]
	v_mfma_f32_16x16x32_bf16 v[16:19], v[148:151], v[230:233], v[16:19]
	v_mfma_f32_16x16x32_bf16 v[12:15], v[178:181], v[230:233], v[12:15]
	v_mfma_f32_16x16x32_bf16 v[64:67], v[152:155], v[194:197], v[64:67]
	v_mfma_f32_16x16x32_bf16 v[60:63], v[186:189], v[194:197], v[60:63]
	v_mfma_f32_16x16x32_bf16 v[48:51], v[152:155], v[202:205], v[48:51]
	v_mfma_f32_16x16x32_bf16 v[44:47], v[186:189], v[202:205], v[44:47]
	v_mfma_f32_16x16x32_bf16 v[32:35], v[152:155], v[226:229], v[32:35]
	v_mfma_f32_16x16x32_bf16 v[28:31], v[186:189], v[226:229], v[28:31]
	v_mfma_f32_16x16x32_bf16 v[16:19], v[152:155], v[234:237], v[16:19]
	v_mfma_f32_16x16x32_bf16 v[12:15], v[186:189], v[234:237], v[12:15]
	s_barrier
	s_setprio 0
	s_add_i32 s28, 0, 0x18000
	s_add_i32 s29, 0, 0x1c000
	v_add_u32_e32 v144, s28, v163
	v_add_u32_e32 v185, s29, v163
	ds_read_b128 v[132:135], v144
	ds_read_b128 v[136:139], v144 offset:1024
	ds_read_b128 v[140:143], v144 offset:2048
	ds_read_b128 v[144:147], v144 offset:3072
	ds_read_b128 v[148:151], v185
	ds_read_b128 v[152:155], v185 offset:1024
	ds_read_b128 v[178:181], v185 offset:2048
	ds_read_b128 v[186:189], v185 offset:3072
	s_add_u32 s26, s26, 0x100000
	s_addc_u32 s27, s27, 0
	s_mov_b32 m0, s51
	v_lshl_add_u64 v[244:245], s[26:27], 0, v[172:173]
	ds_read_b128 v[190:193], v184 offset:32768
	ds_read_b128 v[194:197], v184 offset:33792
	ds_read_b128 v[198:201], v184 offset:34816
	ds_read_b128 v[202:205], v184 offset:35840
	ds_read_b128 v[222:225], v184 offset:36864
	ds_read_b128 v[226:229], v184 offset:37888
	ds_read_b128 v[230:233], v184 offset:38912
	ds_read_b128 v[234:237], v184 offset:39936
	global_load_lds_dwordx4 v[244:245], off
	v_lshl_add_u64 v[244:245], s[26:27], 0, v[170:171]
	s_mov_b32 m0, s54
	s_nop 0
	global_load_lds_dwordx4 v[244:245], off
	s_waitcnt vmcnt(8)
	s_waitcnt lgkmcnt(0)
	s_setprio 1
	s_barrier
	v_mfma_f32_16x16x32_bf16 v[120:123], v[132:135], v[190:193], v[120:123]
	v_mfma_f32_16x16x32_bf16 v[116:119], v[140:143], v[190:193], v[116:119]
	v_mfma_f32_16x16x32_bf16 v[104:107], v[132:135], v[198:201], v[104:107]
	v_mfma_f32_16x16x32_bf16 v[100:103], v[140:143], v[198:201], v[100:103]
	v_mfma_f32_16x16x32_bf16 v[88:91], v[132:135], v[222:225], v[88:91]
	v_mfma_f32_16x16x32_bf16 v[84:87], v[140:143], v[222:225], v[84:87]
	v_mfma_f32_16x16x32_bf16 v[72:75], v[132:135], v[230:233], v[72:75]
	v_mfma_f32_16x16x32_bf16 v[68:71], v[140:143], v[230:233], v[68:71]
	v_mfma_f32_16x16x32_bf16 v[120:123], v[136:139], v[194:197], v[120:123]
	v_mfma_f32_16x16x32_bf16 v[116:119], v[144:147], v[194:197], v[116:119]
	v_mfma_f32_16x16x32_bf16 v[104:107], v[136:139], v[202:205], v[104:107]
	v_mfma_f32_16x16x32_bf16 v[100:103], v[144:147], v[202:205], v[100:103]
	v_mfma_f32_16x16x32_bf16 v[88:91], v[136:139], v[226:229], v[88:91]
	v_mfma_f32_16x16x32_bf16 v[84:87], v[144:147], v[226:229], v[84:87]
	v_mfma_f32_16x16x32_bf16 v[72:75], v[136:139], v[234:237], v[72:75]
	v_mfma_f32_16x16x32_bf16 v[68:71], v[144:147], v[234:237], v[68:71]
	v_mfma_f32_16x16x32_bf16 v[128:131], v[148:151], v[190:193], v[128:131]
	v_mfma_f32_16x16x32_bf16 v[124:127], v[178:181], v[190:193], v[124:127]
	v_mfma_f32_16x16x32_bf16 v[112:115], v[148:151], v[198:201], v[112:115]
	v_mfma_f32_16x16x32_bf16 v[108:111], v[178:181], v[198:201], v[108:111]
	v_mfma_f32_16x16x32_bf16 v[96:99], v[148:151], v[222:225], v[96:99]
	v_mfma_f32_16x16x32_bf16 v[92:95], v[178:181], v[222:225], v[92:95]
	v_mfma_f32_16x16x32_bf16 v[80:83], v[148:151], v[230:233], v[80:83]
	v_mfma_f32_16x16x32_bf16 v[76:79], v[178:181], v[230:233], v[76:79]
	v_mfma_f32_16x16x32_bf16 v[128:131], v[152:155], v[194:197], v[128:131]
	v_mfma_f32_16x16x32_bf16 v[124:127], v[186:189], v[194:197], v[124:127]
	v_mfma_f32_16x16x32_bf16 v[112:115], v[152:155], v[202:205], v[112:115]
	v_mfma_f32_16x16x32_bf16 v[108:111], v[186:189], v[202:205], v[108:111]
	v_mfma_f32_16x16x32_bf16 v[96:99], v[152:155], v[226:229], v[96:99]
	v_mfma_f32_16x16x32_bf16 v[92:95], v[186:189], v[226:229], v[92:95]
	v_mfma_f32_16x16x32_bf16 v[80:83], v[152:155], v[234:237], v[80:83]
	v_mfma_f32_16x16x32_bf16 v[76:79], v[186:189], v[234:237], v[76:79]
	s_barrier
	s_setprio 0
	s_add_i32 s26, s28, s1
	v_lshl_add_u64 v[182:183], v[182:183], 0, s[86:87]
	s_mov_b32 m0, s26
	ds_read_b128 v[190:193], v184 offset:49152
	ds_read_b128 v[194:197], v184 offset:50176
	ds_read_b128 v[198:201], v184 offset:51200
	ds_read_b128 v[202:205], v184 offset:52224
	ds_read_b128 v[222:225], v184 offset:53248
	ds_read_b128 v[226:229], v184 offset:54272
	ds_read_b128 v[230:233], v184 offset:55296
	ds_read_b128 v[234:237], v184 offset:56320
	global_load_lds_dwordx4 v[182:183], off
	s_add_i32 m0, s26, 0x2000
	s_add_u32 s24, s24, 0x100080
	v_lshl_add_u64 v[182:183], v[238:239], 0, s[86:87]
	s_addc_u32 s25, s25, 0
	s_add_i32 s26, s29, s1
	global_load_lds_dwordx4 v[182:183], off
	v_lshl_add_u64 v[182:183], s[24:25], 0, v[2:3]
	s_mov_b32 m0, s26
	s_nop 0
	global_load_lds_dwordx4 v[182:183], off
	v_lshl_add_u64 v[182:183], s[24:25], 0, v[168:169]
	s_add_i32 m0, s26, 0x2000
	s_nop 0
	global_load_lds_dwordx4 v[182:183], off
	v_lshl_add_u64 v[182:183], v[240:241], 0, s[86:87]
	s_mov_b32 m0, s78
	s_nop 0
	global_load_lds_dwordx4 v[182:183], off
	v_lshl_add_u64 v[182:183], v[242:243], 0, s[86:87]
	s_mov_b32 m0, s85
	s_nop 0
	global_load_lds_dwordx4 v[182:183], off
	s_waitcnt vmcnt(8)
	s_waitcnt lgkmcnt(0)
	s_setprio 1
	s_barrier
	v_mfma_f32_16x16x32_bf16 v[56:59], v[132:135], v[190:193], v[56:59]
	v_mfma_f32_16x16x32_bf16 v[52:55], v[140:143], v[190:193], v[52:55]
	v_mfma_f32_16x16x32_bf16 v[40:43], v[132:135], v[198:201], v[40:43]
	v_mfma_f32_16x16x32_bf16 v[36:39], v[140:143], v[198:201], v[36:39]
	v_mfma_f32_16x16x32_bf16 v[24:27], v[132:135], v[222:225], v[24:27]
	v_mfma_f32_16x16x32_bf16 v[20:23], v[140:143], v[222:225], v[20:23]
	v_mfma_f32_16x16x32_bf16 v[8:11], v[132:135], v[230:233], v[8:11]
	v_mfma_f32_16x16x32_bf16 v[4:7], v[140:143], v[230:233], v[4:7]
	v_mfma_f32_16x16x32_bf16 v[56:59], v[136:139], v[194:197], v[56:59]
	v_mfma_f32_16x16x32_bf16 v[52:55], v[144:147], v[194:197], v[52:55]
	v_mfma_f32_16x16x32_bf16 v[40:43], v[136:139], v[202:205], v[40:43]
	v_mfma_f32_16x16x32_bf16 v[36:39], v[144:147], v[202:205], v[36:39]
	v_mfma_f32_16x16x32_bf16 v[24:27], v[136:139], v[226:229], v[24:27]
	v_mfma_f32_16x16x32_bf16 v[20:23], v[144:147], v[226:229], v[20:23]
	v_mfma_f32_16x16x32_bf16 v[8:11], v[136:139], v[234:237], v[8:11]
	v_mfma_f32_16x16x32_bf16 v[4:7], v[144:147], v[234:237], v[4:7]
	v_mfma_f32_16x16x32_bf16 v[64:67], v[148:151], v[190:193], v[64:67]
	v_mfma_f32_16x16x32_bf16 v[60:63], v[178:181], v[190:193], v[60:63]
	v_mfma_f32_16x16x32_bf16 v[48:51], v[148:151], v[198:201], v[48:51]
	v_mfma_f32_16x16x32_bf16 v[44:47], v[178:181], v[198:201], v[44:47]
	v_mfma_f32_16x16x32_bf16 v[32:35], v[148:151], v[222:225], v[32:35]
	v_mfma_f32_16x16x32_bf16 v[28:31], v[178:181], v[222:225], v[28:31]
	v_mfma_f32_16x16x32_bf16 v[16:19], v[148:151], v[230:233], v[16:19]
	v_mfma_f32_16x16x32_bf16 v[12:15], v[178:181], v[230:233], v[12:15]
	v_mfma_f32_16x16x32_bf16 v[64:67], v[152:155], v[194:197], v[64:67]
	v_mfma_f32_16x16x32_bf16 v[60:63], v[186:189], v[194:197], v[60:63]
	v_mfma_f32_16x16x32_bf16 v[48:51], v[152:155], v[202:205], v[48:51]
	v_mfma_f32_16x16x32_bf16 v[44:47], v[186:189], v[202:205], v[44:47]
	v_mfma_f32_16x16x32_bf16 v[32:35], v[152:155], v[226:229], v[32:35]
	v_mfma_f32_16x16x32_bf16 v[28:31], v[186:189], v[226:229], v[28:31]
	v_mfma_f32_16x16x32_bf16 v[16:19], v[152:155], v[234:237], v[16:19]
	s_cmp_eq_u32 s100, 1
	v_mfma_f32_16x16x32_bf16 v[12:15], v[186:189], v[234:237], v[12:15]
	s_cbranch_scc1 .Lnb_lbb0_265
	s_barrier
.Lnb_lbb0_265:
	s_setprio 0
	s_add_i32 s58, s58, 2
	s_add_u32 s6, s6, 0x100
	s_addc_u32 s7, s7, 0
	s_add_u32 s21, s21, 0x100
	s_addc_u32 s13, s13, 0
	s_cmp_gt_u32 s58, 61
	s_cbranch_scc0 .LBB0_265
	s_and_b64 vcc, exec, s[30:31]
	s_cbranch_vccz .LBB0_268
	s_nop 0

.LBB0_1202:
	s_cmp_eq_u32 s58, 60
	s_cselect_b32 s100, 1, 0
	s_cmp_eq_u64 s[14:15], 0
	s_cselect_b32 s101, 1, 0
	s_and_b32 s100, s100, s101
	s_add_u32 s24, s6, 0xfff00080
	s_addc_u32 s25, s7, -1
	s_add_i32 s28, 0, 0x10000
	s_cmp_eq_u32 s58, 60
	s_cselect_b32 s27, s35, s25
	s_cselect_b32 s26, s53, s24
	s_cselect_b32 s25, s31, s13
	s_cselect_b32 s24, s92, s21
	s_add_i32 s71, 0, 0x14000
	v_add_u32_e32 v150, s28, v163
	v_add_u32_e32 v154, s71, v163
	ds_read_b128 v[138:141], v150
	ds_read_b128 v[142:145], v150 offset:1024
	ds_read_b128 v[146:149], v150 offset:2048
	ds_read_b128 v[150:153], v150 offset:3072
	ds_read_b128 v[168:171], v154
	ds_read_b128 v[172:175], v154 offset:1024
	ds_read_b128 v[176:179], v154 offset:2048
	ds_read_b128 v[180:183], v154 offset:3072
	v_lshl_add_u64 v[154:155], s[6:7], 0, v[134:135]
	s_add_i32 m0, s50, 0xc000
	ds_read_b128 v[188:191], v186
	ds_read_b128 v[192:195], v186 offset:1024
	ds_read_b128 v[196:199], v186 offset:2048
	ds_read_b128 v[200:203], v186 offset:3072
	ds_read_b128 v[222:225], v186 offset:4096
	ds_read_b128 v[226:229], v186 offset:5120
	ds_read_b128 v[230:233], v186 offset:6144
	ds_read_b128 v[234:237], v186 offset:7168
	global_load_lds_dwordx4 v[154:155], off
	v_lshl_add_u64 v[154:155], s[6:7], 0, v[136:137]
	s_add_i32 m0, s50, 0xe000
	s_nop 0
	global_load_lds_dwordx4 v[154:155], off
	s_waitcnt vmcnt(8)
	s_waitcnt lgkmcnt(0)
	s_setprio 1
	s_barrier
	v_mfma_f32_16x16x32_bf16 v[128:131], v[138:141], v[188:191], v[128:131]
	v_mfma_f32_16x16x32_bf16 v[124:127], v[146:149], v[188:191], v[124:127]
	v_mfma_f32_16x16x32_bf16 v[112:115], v[138:141], v[196:199], v[112:115]
	v_mfma_f32_16x16x32_bf16 v[108:111], v[146:149], v[196:199], v[108:111]
	v_mfma_f32_16x16x32_bf16 v[96:99], v[138:141], v[222:225], v[96:99]
	v_mfma_f32_16x16x32_bf16 v[92:95], v[146:149], v[222:225], v[92:95]
	v_mfma_f32_16x16x32_bf16 v[80:83], v[138:141], v[230:233], v[80:83]
	v_mfma_f32_16x16x32_bf16 v[76:79], v[146:149], v[230:233], v[76:79]
	v_mfma_f32_16x16x32_bf16 v[128:131], v[142:145], v[192:195], v[128:131]
	v_mfma_f32_16x16x32_bf16 v[124:127], v[150:153], v[192:195], v[124:127]
	v_mfma_f32_16x16x32_bf16 v[112:115], v[142:145], v[200:203], v[112:115]
	v_mfma_f32_16x16x32_bf16 v[108:111], v[150:153], v[200:203], v[108:111]
	v_mfma_f32_16x16x32_bf16 v[96:99], v[142:145], v[226:229], v[96:99]
	v_mfma_f32_16x16x32_bf16 v[92:95], v[150:153], v[226:229], v[92:95]
	v_mfma_f32_16x16x32_bf16 v[80:83], v[142:145], v[234:237], v[80:83]
	v_mfma_f32_16x16x32_bf16 v[76:79], v[150:153], v[234:237], v[76:79]
	v_mfma_f32_16x16x32_bf16 v[120:123], v[168:171], v[188:191], v[120:123]
	v_mfma_f32_16x16x32_bf16 v[116:119], v[176:179], v[188:191], v[116:119]
	v_mfma_f32_16x16x32_bf16 v[104:107], v[168:171], v[196:199], v[104:107]
	v_mfma_f32_16x16x32_bf16 v[100:103], v[176:179], v[196:199], v[100:103]
	v_mfma_f32_16x16x32_bf16 v[88:91], v[168:171], v[222:225], v[88:91]
	v_mfma_f32_16x16x32_bf16 v[84:87], v[176:179], v[222:225], v[84:87]
	v_mfma_f32_16x16x32_bf16 v[72:75], v[168:171], v[230:233], v[72:75]
	v_mfma_f32_16x16x32_bf16 v[68:71], v[176:179], v[230:233], v[68:71]
	v_mfma_f32_16x16x32_bf16 v[120:123], v[172:175], v[192:195], v[120:123]
	v_mfma_f32_16x16x32_bf16 v[116:119], v[180:183], v[192:195], v[116:119]
	v_mfma_f32_16x16x32_bf16 v[104:107], v[172:175], v[200:203], v[104:107]
	v_mfma_f32_16x16x32_bf16 v[100:103], v[180:183], v[200:203], v[100:103]
	v_mfma_f32_16x16x32_bf16 v[88:91], v[172:175], v[226:229], v[88:91]
	v_mfma_f32_16x16x32_bf16 v[84:87], v[180:183], v[226:229], v[84:87]
	v_mfma_f32_16x16x32_bf16 v[72:75], v[172:175], v[234:237], v[72:75]
	v_mfma_f32_16x16x32_bf16 v[68:71], v[180:183], v[234:237], v[68:71]
	s_barrier
	s_setprio 0
	s_add_i32 s28, s28, s46
	v_lshl_add_u64 v[154:155], s[24:25], 0, v[2:3]
	s_mov_b32 m0, s28
	ds_read_b128 v[188:191], v186 offset:16384
	ds_read_b128 v[192:195], v186 offset:17408
	ds_read_b128 v[196:199], v186 offset:18432
	ds_read_b128 v[200:203], v186 offset:19456
	ds_read_b128 v[222:225], v186 offset:20480
	ds_read_b128 v[226:229], v186 offset:21504
	ds_read_b128 v[230:233], v186 offset:22528
	ds_read_b128 v[234:237], v186 offset:23552
	global_load_lds_dwordx4 v[154:155], off
	s_add_i32 m0, s28, 0x2000
	s_add_u32 s28, s24, 0x100000
	v_lshl_add_u64 v[184:185], s[24:25], 0, v[132:133]
	s_addc_u32 s29, s25, 0
	s_add_i32 s71, s71, s46
	global_load_lds_dwordx4 v[184:185], off
	v_lshl_add_u64 v[204:205], s[28:29], 0, v[2:3]
	s_mov_b32 m0, s71
	v_lshl_add_u64 v[238:239], s[26:27], 0, v[132:133]
	global_load_lds_dwordx4 v[204:205], off
	v_lshl_add_u64 v[204:205], s[28:29], 0, v[132:133]
	s_add_i32 m0, s71, 0x2000
	s_nop 0
	global_load_lds_dwordx4 v[204:205], off
	v_lshl_add_u64 v[204:205], s[26:27], 0, v[2:3]
	s_mov_b32 m0, s50
	s_nop 0
	global_load_lds_dwordx4 v[204:205], off
	s_mov_b32 m0, s23
	s_nop 0
	global_load_lds_dwordx4 v[238:239], off
	s_waitcnt vmcnt(8)
	s_waitcnt lgkmcnt(0)
	s_setprio 1
	s_barrier
	v_mfma_f32_16x16x32_bf16 v[64:67], v[138:141], v[188:191], v[64:67]
	v_mfma_f32_16x16x32_bf16 v[60:63], v[146:149], v[188:191], v[60:63]
	v_mfma_f32_16x16x32_bf16 v[48:51], v[138:141], v[196:199], v[48:51]
	v_mfma_f32_16x16x32_bf16 v[44:47], v[146:149], v[196:199], v[44:47]
	v_mfma_f32_16x16x32_bf16 v[32:35], v[138:141], v[222:225], v[32:35]
	v_mfma_f32_16x16x32_bf16 v[28:31], v[146:149], v[222:225], v[28:31]
	v_mfma_f32_16x16x32_bf16 v[16:19], v[138:141], v[230:233], v[16:19]
	v_mfma_f32_16x16x32_bf16 v[12:15], v[146:149], v[230:233], v[12:15]
	v_mfma_f32_16x16x32_bf16 v[64:67], v[142:145], v[192:195], v[64:67]
	v_mfma_f32_16x16x32_bf16 v[60:63], v[150:153], v[192:195], v[60:63]
	v_mfma_f32_16x16x32_bf16 v[48:51], v[142:145], v[200:203], v[48:51]
	v_mfma_f32_16x16x32_bf16 v[44:47], v[150:153], v[200:203], v[44:47]
	v_mfma_f32_16x16x32_bf16 v[32:35], v[142:145], v[226:229], v[32:35]
	v_mfma_f32_16x16x32_bf16 v[28:31], v[150:153], v[226:229], v[28:31]
	v_mfma_f32_16x16x32_bf16 v[16:19], v[142:145], v[234:237], v[16:19]
	v_mfma_f32_16x16x32_bf16 v[12:15], v[150:153], v[234:237], v[12:15]
	v_mfma_f32_16x16x32_bf16 v[56:59], v[168:171], v[188:191], v[56:59]
	v_mfma_f32_16x16x32_bf16 v[52:55], v[176:179], v[188:191], v[52:55]
	v_mfma_f32_16x16x32_bf16 v[40:43], v[168:171], v[196:199], v[40:43]
	v_mfma_f32_16x16x32_bf16 v[36:39], v[176:179], v[196:199], v[36:39]
	v_mfma_f32_16x16x32_bf16 v[24:27], v[168:171], v[222:225], v[24:27]
	v_mfma_f32_16x16x32_bf16 v[20:23], v[176:179], v[222:225], v[20:23]
	v_mfma_f32_16x16x32_bf16 v[8:11], v[168:171], v[230:233], v[8:11]
	v_mfma_f32_16x16x32_bf16 v[4:7], v[176:179], v[230:233], v[4:7]
	v_mfma_f32_16x16x32_bf16 v[56:59], v[172:175], v[192:195], v[56:59]
	v_mfma_f32_16x16x32_bf16 v[52:55], v[180:183], v[192:195], v[52:55]
	v_mfma_f32_16x16x32_bf16 v[40:43], v[172:175], v[200:203], v[40:43]
	v_mfma_f32_16x16x32_bf16 v[36:39], v[180:183], v[200:203], v[36:39]
	v_mfma_f32_16x16x32_bf16 v[24:27], v[172:175], v[226:229], v[24:27]
	v_mfma_f32_16x16x32_bf16 v[20:23], v[180:183], v[226:229], v[20:23]
	v_mfma_f32_16x16x32_bf16 v[8:11], v[172:175], v[234:237], v[8:11]
	v_mfma_f32_16x16x32_bf16 v[4:7], v[180:183], v[234:237], v[4:7]
	s_barrier
	s_setprio 0
	s_add_i32 s28, 0, 0x18000
	s_add_i32 s29, 0, 0x1c000
	v_add_u32_e32 v150, s28, v163
	v_add_u32_e32 v180, s29, v163
	ds_read_b128 v[138:141], v150
	ds_read_b128 v[142:145], v150 offset:1024
	ds_read_b128 v[146:149], v150 offset:2048
	ds_read_b128 v[150:153], v150 offset:3072
	ds_read_b128 v[168:171], v180
	ds_read_b128 v[172:175], v180 offset:1024
	ds_read_b128 v[176:179], v180 offset:2048
	ds_read_b128 v[180:183], v180 offset:3072
	s_add_u32 s26, s26, 0x100000
	s_addc_u32 s27, s27, 0
	s_mov_b32 m0, s51
	v_lshl_add_u64 v[240:241], s[26:27], 0, v[2:3]
	ds_read_b128 v[188:191], v186 offset:32768
	ds_read_b128 v[192:195], v186 offset:33792
	ds_read_b128 v[196:199], v186 offset:34816
	ds_read_b128 v[200:203], v186 offset:35840
	ds_read_b128 v[222:225], v186 offset:36864
	ds_read_b128 v[226:229], v186 offset:37888
	ds_read_b128 v[230:233], v186 offset:38912
	ds_read_b128 v[234:237], v186 offset:39936
	global_load_lds_dwordx4 v[240:241], off
	v_lshl_add_u64 v[240:241], s[26:27], 0, v[132:133]
	s_mov_b32 m0, s54
	s_nop 0
	global_load_lds_dwordx4 v[240:241], off
	s_waitcnt vmcnt(8)
	s_waitcnt lgkmcnt(0)
	s_setprio 1
	s_barrier
	v_mfma_f32_16x16x32_bf16 v[128:131], v[138:141], v[188:191], v[128:131]
	v_mfma_f32_16x16x32_bf16 v[124:127], v[146:149], v[188:191], v[124:127]
	v_mfma_f32_16x16x32_bf16 v[112:115], v[138:141], v[196:199], v[112:115]
	v_mfma_f32_16x16x32_bf16 v[108:111], v[146:149], v[196:199], v[108:111]
	v_mfma_f32_16x16x32_bf16 v[96:99], v[138:141], v[222:225], v[96:99]
	v_mfma_f32_16x16x32_bf16 v[92:95], v[146:149], v[222:225], v[92:95]
	v_mfma_f32_16x16x32_bf16 v[80:83], v[138:141], v[230:233], v[80:83]
	v_mfma_f32_16x16x32_bf16 v[76:79], v[146:149], v[230:233], v[76:79]
	v_mfma_f32_16x16x32_bf16 v[128:131], v[142:145], v[192:195], v[128:131]
	v_mfma_f32_16x16x32_bf16 v[124:127], v[150:153], v[192:195], v[124:127]
	v_mfma_f32_16x16x32_bf16 v[112:115], v[142:145], v[200:203], v[112:115]
	v_mfma_f32_16x16x32_bf16 v[108:111], v[150:153], v[200:203], v[108:111]
	v_mfma_f32_16x16x32_bf16 v[96:99], v[142:145], v[226:229], v[96:99]
	v_mfma_f32_16x16x32_bf16 v[92:95], v[150:153], v[226:229], v[92:95]
	v_mfma_f32_16x16x32_bf16 v[80:83], v[142:145], v[234:237], v[80:83]
	v_mfma_f32_16x16x32_bf16 v[76:79], v[150:153], v[234:237], v[76:79]
	v_mfma_f32_16x16x32_bf16 v[120:123], v[168:171], v[188:191], v[120:123]
	v_mfma_f32_16x16x32_bf16 v[116:119], v[176:179], v[188:191], v[116:119]
	v_mfma_f32_16x16x32_bf16 v[104:107], v[168:171], v[196:199], v[104:107]
	v_mfma_f32_16x16x32_bf16 v[100:103], v[176:179], v[196:199], v[100:103]
	v_mfma_f32_16x16x32_bf16 v[88:91], v[168:171], v[222:225], v[88:91]
	v_mfma_f32_16x16x32_bf16 v[84:87], v[176:179], v[222:225], v[84:87]
	v_mfma_f32_16x16x32_bf16 v[72:75], v[168:171], v[230:233], v[72:75]
	v_mfma_f32_16x16x32_bf16 v[68:71], v[176:179], v[230:233], v[68:71]
	v_mfma_f32_16x16x32_bf16 v[120:123], v[172:175], v[192:195], v[120:123]
	v_mfma_f32_16x16x32_bf16 v[116:119], v[180:183], v[192:195], v[116:119]
	v_mfma_f32_16x16x32_bf16 v[104:107], v[172:175], v[200:203], v[104:107]
	v_mfma_f32_16x16x32_bf16 v[100:103], v[180:183], v[200:203], v[100:103]
	v_mfma_f32_16x16x32_bf16 v[88:91], v[172:175], v[226:229], v[88:91]
	v_mfma_f32_16x16x32_bf16 v[84:87], v[180:183], v[226:229], v[84:87]
	v_mfma_f32_16x16x32_bf16 v[72:75], v[172:175], v[234:237], v[72:75]
	v_mfma_f32_16x16x32_bf16 v[68:71], v[180:183], v[234:237], v[68:71]
	s_barrier
	s_setprio 0
	s_add_i32 s26, s28, s46
	v_lshl_add_u64 v[154:155], v[154:155], 0, s[86:87]
	s_mov_b32 m0, s26
	ds_read_b128 v[188:191], v186 offset:49152
	ds_read_b128 v[192:195], v186 offset:50176
	ds_read_b128 v[196:199], v186 offset:51200
	ds_read_b128 v[200:203], v186 offset:52224
	ds_read_b128 v[222:225], v186 offset:53248
	ds_read_b128 v[226:229], v186 offset:54272
	ds_read_b128 v[230:233], v186 offset:55296
	ds_read_b128 v[234:237], v186 offset:56320
	global_load_lds_dwordx4 v[154:155], off
	s_add_i32 m0, s26, 0x2000
	s_add_u32 s24, s24, 0x100080
	v_lshl_add_u64 v[154:155], v[184:185], 0, s[86:87]
	s_addc_u32 s25, s25, 0
	s_add_i32 s26, s29, s46
	global_load_lds_dwordx4 v[154:155], off
	v_lshl_add_u64 v[154:155], s[24:25], 0, v[2:3]
	s_mov_b32 m0, s26
	s_nop 0
	global_load_lds_dwordx4 v[154:155], off
	v_lshl_add_u64 v[154:155], s[24:25], 0, v[132:133]
	s_add_i32 m0, s26, 0x2000
	s_nop 0
	global_load_lds_dwordx4 v[154:155], off
	v_lshl_add_u64 v[154:155], v[204:205], 0, s[86:87]
	s_mov_b32 m0, s76
	s_nop 0
	global_load_lds_dwordx4 v[154:155], off
	v_lshl_add_u64 v[154:155], v[238:239], 0, s[86:87]
	s_mov_b32 m0, s77
	s_nop 0
	global_load_lds_dwordx4 v[154:155], off
	s_waitcnt vmcnt(8)
	s_waitcnt lgkmcnt(0)
	s_setprio 1
	s_barrier
	v_mfma_f32_16x16x32_bf16 v[64:67], v[138:141], v[188:191], v[64:67]
	v_mfma_f32_16x16x32_bf16 v[60:63], v[146:149], v[188:191], v[60:63]
	v_mfma_f32_16x16x32_bf16 v[48:51], v[138:141], v[196:199], v[48:51]
	v_mfma_f32_16x16x32_bf16 v[44:47], v[146:149], v[196:199], v[44:47]
	v_mfma_f32_16x16x32_bf16 v[32:35], v[138:141], v[222:225], v[32:35]
	v_mfma_f32_16x16x32_bf16 v[28:31], v[146:149], v[222:225], v[28:31]
	v_mfma_f32_16x16x32_bf16 v[16:19], v[138:141], v[230:233], v[16:19]
	v_mfma_f32_16x16x32_bf16 v[12:15], v[146:149], v[230:233], v[12:15]
	v_mfma_f32_16x16x32_bf16 v[64:67], v[142:145], v[192:195], v[64:67]
	v_mfma_f32_16x16x32_bf16 v[60:63], v[150:153], v[192:195], v[60:63]
	v_mfma_f32_16x16x32_bf16 v[48:51], v[142:145], v[200:203], v[48:51]
	v_mfma_f32_16x16x32_bf16 v[44:47], v[150:153], v[200:203], v[44:47]
	v_mfma_f32_16x16x32_bf16 v[32:35], v[142:145], v[226:229], v[32:35]
	v_mfma_f32_16x16x32_bf16 v[28:31], v[150:153], v[226:229], v[28:31]
	v_mfma_f32_16x16x32_bf16 v[16:19], v[142:145], v[234:237], v[16:19]
	v_mfma_f32_16x16x32_bf16 v[12:15], v[150:153], v[234:237], v[12:15]
	v_mfma_f32_16x16x32_bf16 v[56:59], v[168:171], v[188:191], v[56:59]
	v_mfma_f32_16x16x32_bf16 v[52:55], v[176:179], v[188:191], v[52:55]
	v_mfma_f32_16x16x32_bf16 v[40:43], v[168:171], v[196:199], v[40:43]
	v_mfma_f32_16x16x32_bf16 v[36:39], v[176:179], v[196:199], v[36:39]
	v_mfma_f32_16x16x32_bf16 v[24:27], v[168:171], v[222:225], v[24:27]
	v_mfma_f32_16x16x32_bf16 v[20:23], v[176:179], v[222:225], v[20:23]
	v_mfma_f32_16x16x32_bf16 v[8:11], v[168:171], v[230:233], v[8:11]
	v_mfma_f32_16x16x32_bf16 v[4:7], v[176:179], v[230:233], v[4:7]
	v_mfma_f32_16x16x32_bf16 v[56:59], v[172:175], v[192:195], v[56:59]
	v_mfma_f32_16x16x32_bf16 v[52:55], v[180:183], v[192:195], v[52:55]
	v_mfma_f32_16x16x32_bf16 v[40:43], v[172:175], v[200:203], v[40:43]
	v_mfma_f32_16x16x32_bf16 v[36:39], v[180:183], v[200:203], v[36:39]
	v_mfma_f32_16x16x32_bf16 v[24:27], v[172:175], v[226:229], v[24:27]
	v_mfma_f32_16x16x32_bf16 v[20:23], v[180:183], v[226:229], v[20:23]
	v_mfma_f32_16x16x32_bf16 v[8:11], v[172:175], v[234:237], v[8:11]
	s_cmp_eq_u32 s100, 1
	v_mfma_f32_16x16x32_bf16 v[4:7], v[180:183], v[234:237], v[4:7]
	s_cbranch_scc1 .Lnb_lbb0_1202
	s_barrier
.Lnb_lbb0_1202:
	s_setprio 0
	s_add_i32 s58, s58, 2
	s_add_u32 s6, s6, 0x100
	s_addc_u32 s7, s7, 0
	s_add_u32 s21, s21, 0x100
	s_addc_u32 s13, s13, 0
	s_cmp_gt_u32 s58, 61
	s_cbranch_scc0 .LBB0_1202
	s_and_b64 vcc, exec, s[14:15]
	s_cbranch_vccz .LBB0_1205
	s_nop 0
